# baseline (speedup 1.0000x reference)
_Z16bilateral_kernelPKfS0_Pf:
	s_load_dwordx2 s[4:5], s[0:1], 0x0
	s_load_dwordx2 s[8:9], s[0:1], 0x10
	s_lshr_b32 s19, s2, 8
	s_and_b32 s0, s2, 7
	s_mulk_i32 s0, 0x60
	s_lshr_b32 s1, s2, 3
	s_add_i32 s1, s0, s1
	s_lshr_b32 s0, s1, 6
	s_lshl_b32 s11, s1, 6
	s_nop 0
	s_and_b32 s11, s11, 0x1c0
	s_lshl_b32 s1, s1, 3
	s_nop 0
	s_and_b32 s10, s1, 0x1c0
	s_mov_b32 s1, 0
	s_lshl_b64 s[2:3], s[0:1], 20
	s_mov_b32 s20, 0xc05dfbe6
	s_mov_b32 s21, 0xc05dfbe6
	s_mov_b32 s22, 0xc0a8390e
	s_mov_b32 s23, 0xc0a8390e
	s_mov_b32 s24, 0xc08211a7
	s_mov_b32 s25, 0xc08211a7
	s_mov_b32 s26, 0xc0bb4cc1
	s_mov_b32 s27, 0xc0bb4cc1
	s_mov_b32 s28, 0xc0f487dc
	s_mov_b32 s29, 0xc0f487dc
	s_mov_b32 s30, 0x3e0bd796
	s_mov_b32 s31, 0x3e0bd796
	s_mov_b32 s32, 0x3f45a90c
	s_mov_b32 s33, 0x3f45a90c
	s_mov_b32 s34, 0x3fa5c782
	s_mov_b32 s35, 0x3fa5c782
	v_and_b32_e32 v118, 15, v0
	v_lshrrev_b32_e32 v115, 2, v0
	v_lshl_or_b32 v113, v118, 2, s11
	v_and_or_b32 v117, v115, 60, s10
	v_min_u32_e32 v116, 0x1fa, v113
	v_sub_u32_e64 v115, v113, 2 clamp
	v_add_u32_e64 v116, 4, v116
	v_cmp_eq_u32_e64 s[16:17], 0, v118
	v_cmp_eq_u32_e32 vcc, 15, v118
	s_nop 1
	v_cndmask_b32_e64 v115, v116, v115, s[16:17]
	s_or_b64 vcc, s[16:17], vcc
	v_lshlrev_b32_e32 v115, 2, v115
	v_mov_b32_e32 v116, 0x7ff00000
	s_nop 0
	v_cndmask_b32_e32 v112, v116, v115, vcc
	s_movk_i32 s18, 0x1fc
	v_cmp_eq_u32_e32 vcc, 0, v113
	v_cmp_eq_u32_e64 s[16:17], s18, v113
	v_lshlrev_b32_e32 v113, 2, v113
	s_waitcnt lgkmcnt(0)
	s_add_u32 s4, s4, s2
	s_addc_u32 s5, s5, s3
	s_and_b32 s5, s5, 0xffff
	s_mov_b32 s6, 0x100000
	s_mov_b32 s7, 0x20000
	s_add_u32 s12, s8, s2
	s_addc_u32 s13, s9, s3
	s_and_b32 s13, s13, 0xffff
	s_mov_b32 s14, 0x100000
	s_mov_b32 s15, 0x20000
	s_cmp_eq_u32 s19, 0
	s_cbranch_scc1 .Lmynosl
	s_sleep 12
	s_cmp_eq_u32 s19, 1
	s_cbranch_scc1 .Lmynosl
	s_sleep 12
